# attention: light waves (0-3) delay the start of each active tile by s_sleep 10 so that their QK MFMAs do not collide with the heavy partner wave, on top of best
# speedup vs baseline: 1.0032x; 1.0021x over previous
; #define LAS __attribute__((address_space(3)))
; #define SBAR() __builtin_amdgcn_sched_barrier(0)
; __device__ __forceinline__ void qkt(f32x16& p0, f32x16& p1, LAS unsigned char* lds  , int r32, int hi, const bf16x8* qr) {
;     p0 = f32x16{}; p1 = f32x16{};
;     const LAS unsigned char* kb[4];
; #pragma unroll
;     for (int dd = 0; dd < 4; ++dd) kb[dd] = lds + K_OFF + KSWZ(r32, (dd * 16 + hi * 8) * 2);
; #pragma unroll
;     for (int d0 = 0; d0 < 8; ++d0) { const LAS unsigned char* a = kb[d0 & 3] + (d0 >> 2) * 128;
;         const bf16x8 b0 = *(const LAS bf16x8*)(a);
;         const bf16x8 b1 = *(const LAS bf16x8*)(a + 32 * 256);
;         p0 = __builtin_amdgcn_mfma_f32_32x32x16_bf16(b0, qr[d0], p0, 0, 0, 0);
;         p1 = __builtin_amdgcn_mfma_f32_32x32x16_bf16(b1, qr[d0], p1, 0, 0, 0); }
; #pragma unroll
;     for (int e = 0; e < 4; ++e) { const LAS unsigned char* a = lds + P_OFF + KPSWZ(r32, (e * 2 + hi) * 16);
;         const bf16x8 b0 = *(const LAS bf16x8*)(a);
;         const bf16x8 b1 = *(const LAS bf16x8*)(a + 32 * 128);
;         p0 = __builtin_amdgcn_mfma_f32_32x32x16_bf16(b0, qr[8 + e], p0, 0, 0, 0);
;         p1 = __builtin_amdgcn_mfma_f32_32x32x16_bf16(b1, qr[8 + e], p1, 0, 0, 0); }
; }
; __device__ __forceinline__ void attn_unit(LAS unsigned char* lds, int b, int h, int qb, const bf16* Q  , const bf16* KV  , const bf16* KPE  ,
;                                           const float* ROPE  , bf16* O  , const int wave_) {
;     ...
;     for (int t = 0; t < NT; ++t) {
;         asm volatile("s_waitcnt vmcnt(5)" ::: "memory"); __builtin_amdgcn_s_barrier();
;         { const int tn = (t + 2 < NT) ? t + 2 : NT - 1; AISSUE(tn, bl); }
;         const int kb_ = t * KVBLK;
;         if (kb_ <= qlo + 31) {
;             SBAR(); qkt(p0, p1, lds + bc, r32, hi, qr);
;             if (kb_ + KVBLK - 1 > qlo) mask_tile(p0, p1, qm - kb_);
.LBB0_720:
	s_add_i32 s4, s73, 2
	s_min_u32 s70, s4, s2
	s_lshl_b64 s[4:5], s[70:71], 18
	s_add_u32 s4, s96, s4
	s_addc_u32 s5, s97, s5
	v_lshl_add_u64 v[64:65], v[150:151], 1, s[4:5]
	s_add_i32 s8, s95, s69
	v_lshl_add_u64 v[64:65], v[64:65], 0, s[66:67]
	s_mov_b32 m0, s8
	s_waitcnt vmcnt(5)
	s_barrier
	global_load_lds_dwordx4 v[64:65], off
	v_lshl_add_u64 v[64:65], v[152:153], 1, s[4:5]
	v_lshl_add_u64 v[64:65], v[64:65], 0, s[66:67]
	s_add_i32 m0, s8, 0x2000
	s_lshl_b64 s[6:7], s[70:71], 13
	global_load_lds_dwordx4 v[64:65], off
	v_lshl_add_u64 v[64:65], v[146:147], 1, s[4:5]
	s_add_i32 m0, s8, 0x4000
	s_nop 0
	global_load_lds_dwordx4 v[64:65], off
	v_lshl_add_u64 v[64:65], v[148:149], 1, s[4:5]
	s_add_i32 m0, s8, 0x6000
	s_sub_i32 s4, s94, 63
	global_load_lds_dwordx4 v[64:65], off
	v_lshl_add_u64 v[64:65], v[154:155], 0, s[6:7]
	s_add_i32 m0, s8, 0x8000
	s_cmp_gt_i32 s4, s68
	global_load_lds_dwordx4 v[64:65], off
	s_cbranch_scc1 .LBB0_728
	v_readlane_b32 s4, v254, 60
	s_nop 3
	s_cmp_gt_u32 s4, 3
	s_cbranch_scc1 .Lattn_nodelay
	s_sleep 10
.Lattn_nodelay:
	s_add_i32 s4, s72, 0
	v_add_u32_e32 v174, s4, v160
	v_add_u32_e32 v68, v174, v161
	ds_read_b128 v[64:67], v68 offset:16384
	ds_read_b128 v[176:179], v68 offset:16512
	v_add_u32_e32 v192, v174, v162
	v_add_u32_e32 v200, v174, v163
	v_add_u32_e32 v174, v174, v165
	s_waitcnt lgkmcnt(0)
	v_mfma_f32_32x32x16_bf16 v[80:95], v[64:67], v[124:127], 0
	ds_read_b128 v[64:67], v68 offset:24576
	ds_read_b128 v[180:183], v68 offset:24704
	ds_read_b128 v[184:187], v192 offset:16384
	ds_read_b128 v[188:191], v192 offset:16512
	s_cmp_le_i32 s94, s33
	s_waitcnt lgkmcnt(0)
	v_mfma_f32_32x32x16_bf16 v[80:95], v[184:187], v[100:103], v[80:95]
	ds_read_b128 v[184:187], v192 offset:24576
	ds_read_b128 v[192:195], v192 offset:24704
	v_mfma_f32_32x32x16_bf16 v[64:79], v[64:67], v[124:127], 0
	s_waitcnt lgkmcnt(0)
	v_mfma_f32_32x32x16_bf16 v[64:79], v[184:187], v[100:103], v[64:79]
	ds_read_b128 v[184:187], v200 offset:16384
	ds_read_b128 v[196:199], v200 offset:16512
	s_waitcnt lgkmcnt(0)
	v_mfma_f32_32x32x16_bf16 v[80:95], v[184:187], v[104:107], v[80:95]
	ds_read_b128 v[184:187], v200 offset:24576
	ds_read_b128 v[200:203], v200 offset:24704
	s_waitcnt lgkmcnt(0)
	v_mfma_f32_32x32x16_bf16 v[64:79], v[184:187], v[104:107], v[64:79]
	ds_read_b128 v[184:187], v174 offset:16384
	ds_read_b128 v[204:207], v174 offset:16512
	s_waitcnt lgkmcnt(0)
	v_mfma_f32_32x32x16_bf16 v[80:95], v[184:187], v[108:111], v[80:95]
	ds_read_b128 v[184:187], v174 offset:24576
	ds_read_b128 v[208:211], v174 offset:24704
	v_add_u32_e32 v174, s4, v166
	s_waitcnt lgkmcnt(0)
	v_mfma_f32_32x32x16_bf16 v[64:79], v[184:187], v[108:111], v[64:79]
	v_mfma_f32_32x32x16_bf16 v[80:95], v[176:179], v[112:115], v[80:95]
	v_mfma_f32_32x32x16_bf16 v[64:79], v[180:183], v[112:115], v[64:79]
	v_add_u32_e32 v180, v174, v167
	ds_read_b128 v[176:179], v180 offset:32768
	ds_read_b128 v[180:183], v180 offset:36864
	v_mfma_f32_32x32x16_bf16 v[80:95], v[188:191], v[116:119], v[80:95]
	v_mfma_f32_32x32x16_bf16 v[64:79], v[192:195], v[116:119], v[64:79]
	v_mfma_f32_32x32x16_bf16 v[80:95], v[196:199], v[120:123], v[80:95]
	v_mfma_f32_32x32x16_bf16 v[64:79], v[200:203], v[120:123], v[64:79]
	v_mfma_f32_32x32x16_bf16 v[80:95], v[204:207], v[96:99], v[80:95]
	v_mfma_f32_32x32x16_bf16 v[64:79], v[208:211], v[96:99], v[64:79]
	s_waitcnt lgkmcnt(0)
	v_mfma_f32_32x32x16_bf16 v[80:95], v[176:179], v[128:131], v[80:95]
	v_mfma_f32_32x32x16_bf16 v[64:79], v[180:183], v[128:131], v[64:79]
	v_add_u32_e32 v180, v174, v168
	ds_read_b128 v[176:179], v180 offset:32768
	ds_read_b128 v[180:183], v180 offset:36864
	s_waitcnt lgkmcnt(0)
	v_mfma_f32_32x32x16_bf16 v[80:95], v[176:179], v[136:139], v[80:95]
	v_mfma_f32_32x32x16_bf16 v[64:79], v[180:183], v[136:139], v[64:79]
	v_add_u32_e32 v180, v174, v169
	ds_read_b128 v[176:179], v180 offset:32768
	ds_read_b128 v[180:183], v180 offset:36864
	v_add_u32_e32 v174, v174, v170
	s_waitcnt lgkmcnt(0)
	v_mfma_f32_32x32x16_bf16 v[80:95], v[176:179], v[132:135], v[80:95]
	v_mfma_f32_32x32x16_bf16 v[64:79], v[180:183], v[132:135], v[64:79]
	ds_read_b128 v[176:179], v174 offset:32768
	ds_read_b128 v[180:183], v174 offset:36864
	s_waitcnt lgkmcnt(0)
	v_mfma_f32_32x32x16_bf16 v[80:95], v[176:179], v[140:143], v[80:95]
	v_mfma_f32_32x32x16_bf16 v[64:79], v[180:183], v[140:143], v[64:79]
	s_cbranch_scc1 .LBB0_723
; __device__ __forceinline__ void mask_tile(f32x16& p0, f32x16& p1, int dq) {
;     const float NEG = -__builtin_inff();
; #pragma unroll
;     for (int r = 0; r < 16; ++r) { const int c = (r & 3) + 8 * (r >> 2);
;         if (dq - c < 0) p0[r] = NEG;
;         if (dq - c - 32 < 0) p1[r] = NEG; }
; }
	v_cmp_gt_i32_e64 s[62:63], 26, v172
	v_cmp_gt_i32_e64 s[64:65], 27, v172
	v_cmp_gt_i32_e64 s[60:61], 25, v172
	s_and_b64 s[62:63], s[64:65], s[62:63]
	v_cmp_gt_i32_e64 s[58:59], 24, v172
	s_and_b64 s[60:61], s[62:63], s[60:61]
	v_cmp_gt_i32_e64 s[56:57], 19, v172
	s_and_b64 s[58:59], s[60:61], s[58:59]
	v_cmp_gt_i32_e64 s[54:55], 18, v172
	s_and_b64 s[56:57], s[58:59], s[56:57]
	v_cmp_gt_i32_e64 s[52:53], 17, v172
	s_and_b64 s[54:55], s[56:57], s[54:55]
	v_cmp_gt_i32_e64 s[50:51], 16, v172
	s_and_b64 s[52:53], s[54:55], s[52:53]
	v_cmp_gt_i32_e64 s[48:49], 11, v172
	s_and_b64 s[50:51], s[52:53], s[50:51]
	v_cmp_gt_i32_e64 s[46:47], 10, v172
	s_and_b64 s[48:49], s[50:51], s[48:49]
	v_cmp_gt_i32_e64 s[44:45], 9, v172
	s_and_b64 s[46:47], s[48:49], s[46:47]
	v_cmp_gt_i32_e64 s[42:43], 8, v172
	s_and_b64 s[44:45], s[46:47], s[44:45]
	v_cmp_gt_i32_e64 s[40:41], 3, v172
	s_and_b64 s[42:43], s[44:45], s[42:43]
	v_cmp_gt_i32_e64 s[38:39], 2, v172
	s_and_b64 s[40:41], s[42:43], s[40:41]
	v_cmp_gt_i32_e64 s[36:37], 1, v172
	s_and_b64 s[38:39], s[40:41], s[38:39]
	v_cmp_gt_i32_e64 s[34:35], 0, v172
	s_and_b64 s[36:37], s[38:39], s[36:37]
	s_and_b64 s[34:35], s[36:37], s[34:35]
	v_cmp_gt_i32_e64 s[30:31], 58, v172
	v_cndmask_b32_e64 v80, v80, v173, s[34:35]
	v_cmp_gt_i32_e64 s[34:35], 59, v172
	v_cmp_gt_i32_e64 s[28:29], 57, v172
	s_and_b64 s[30:31], s[34:35], s[30:31]
	v_cmp_gt_i32_e64 s[26:27], 56, v172
	s_and_b64 s[28:29], s[30:31], s[28:29]
	v_cmp_gt_i32_e64 s[24:25], 51, v172
	s_and_b64 s[26:27], s[28:29], s[26:27]
	v_cmp_gt_i32_e64 s[22:23], 50, v172
	s_and_b64 s[24:25], s[26:27], s[24:25]
	v_cmp_gt_i32_e64 s[20:21], 49, v172
	s_and_b64 s[22:23], s[24:25], s[22:23]
	v_cmp_gt_i32_e64 s[18:19], 48, v172
	s_and_b64 s[20:21], s[22:23], s[20:21]
	v_cmp_gt_i32_e64 s[16:17], 43, v172
	s_and_b64 s[18:19], s[20:21], s[18:19]
	v_cmp_gt_i32_e64 s[14:15], 42, v172
	s_and_b64 s[16:17], s[18:19], s[16:17]
	v_cmp_gt_i32_e64 s[12:13], 41, v172
	s_and_b64 s[14:15], s[16:17], s[14:15]
	v_cmp_gt_i32_e64 s[10:11], 40, v172
	s_and_b64 s[12:13], s[14:15], s[12:13]
	v_cmp_gt_i32_e64 s[8:9], 35, v172
	s_and_b64 s[10:11], s[12:13], s[10:11]
	v_cmp_gt_i32_e64 s[6:7], 34, v172
	s_and_b64 s[8:9], s[10:11], s[8:9]
	v_cmp_gt_i32_e64 s[4:5], 33, v172
	v_cndmask_b32_e64 v94, v94, v173, s[62:63]
	v_cndmask_b32_e64 v93, v93, v173, s[60:61]
	v_cndmask_b32_e64 v92, v92, v173, s[58:59]
	v_cndmask_b32_e64 v91, v91, v173, s[56:57]
	v_cndmask_b32_e64 v90, v90, v173, s[54:55]
	v_cndmask_b32_e64 v89, v89, v173, s[52:53]
	v_cndmask_b32_e64 v88, v88, v173, s[50:51]
	v_cndmask_b32_e64 v87, v87, v173, s[48:49]
	v_readlane_b32 s48, v254, 42
	s_and_b64 s[6:7], s[8:9], s[6:7]
	v_cmp_gt_i32_e32 vcc, 32, v172
	v_readlane_b32 s52, v254, 46
	v_readlane_b32 s53, v254, 47
	v_readlane_b32 s56, v254, 50
	v_readlane_b32 s57, v254, 51
	v_readlane_b32 s58, v254, 52
	v_readlane_b32 s59, v254, 53
	v_readlane_b32 s60, v254, 54
	v_readlane_b32 s61, v254, 55
	s_and_b64 s[4:5], s[6:7], s[4:5]
	v_readlane_b32 s62, v254, 56
	v_readlane_b32 s63, v254, 57
	s_mov_b64 s[52:53], s[56:57]
	s_mov_b64 s[56:57], s[60:61]
	s_and_b64 vcc, s[4:5], vcc
	v_cndmask_b32_e64 v95, v95, v173, s[64:65]
	s_mov_b64 s[58:59], s[62:63]
	v_cndmask_b32_e64 v86, v86, v173, s[46:47]
	v_cndmask_b32_e64 v85, v85, v173, s[44:45]
	v_cndmask_b32_e64 v84, v84, v173, s[42:43]
	v_cndmask_b32_e64 v83, v83, v173, s[40:41]
	v_cndmask_b32_e64 v82, v82, v173, s[38:39]
	v_cndmask_b32_e64 v81, v81, v173, s[36:37]
	v_cndmask_b32_e64 v79, v79, v173, s[34:35]
	v_cndmask_b32_e64 v78, v78, v173, s[30:31]
	v_cndmask_b32_e64 v77, v77, v173, s[28:29]
	v_cndmask_b32_e64 v76, v76, v173, s[26:27]
	v_cndmask_b32_e64 v75, v75, v173, s[24:25]
	v_cndmask_b32_e64 v74, v74, v173, s[22:23]
	v_cndmask_b32_e64 v73, v73, v173, s[20:21]
	v_cndmask_b32_e64 v72, v72, v173, s[18:19]
	v_cndmask_b32_e64 v71, v71, v173, s[16:17]
	v_cndmask_b32_e64 v70, v70, v173, s[14:15]
	v_cndmask_b32_e64 v69, v69, v173, s[12:13]
	v_cndmask_b32_e64 v68, v68, v173, s[10:11]
	v_cndmask_b32_e64 v67, v67, v173, s[8:9]
	v_cndmask_b32_e64 v66, v66, v173, s[6:7]
	v_cndmask_b32_e64 v65, v65, v173, s[4:5]
	v_cndmask_b32_e32 v64, v64, v173, vcc
	v_readlane_b32 s49, v254, 43
	v_readlane_b32 s50, v254, 44
	v_readlane_b32 s51, v254, 45
	v_readlane_b32 s54, v254, 48
	v_readlane_b32 s55, v254, 49
